# baseline (speedup 1.0000x reference)
.Lapf_skip_a:
	s_waitcnt lgkmcnt(0)
	s_barrier
	s_branch .LBB3_63
	s_nop 0
	s_nop 0
	s_nop 0
